# U3f: s_setprio 3 for the 14 blocks whose waves take a second tile, so the tail starts earlier
# baseline (speedup 1.0000x reference)
.LBB9_2:
	s_or_b64 exec, exec, s[6:7]
	s_waitcnt lgkmcnt(0)
	s_barrier
	s_mov_b32 s30, s2
	v_mov_b32_e32 v77, v0
	v_mov_b32_e32 v79, v10
	s_mov_b32 s31, 0
	s_cmpk_ge_u32 s2, 14
	s_cbranch_scc1 .Lu3_nopri
	s_setprio 3
.Lu3_nopri:
.Lu3_again:
	s_load_dword s3, s[0:1], 0x58
	v_lshrrev_b32_e32 v1, 6, v0
	s_waitcnt lgkmcnt(0)
	v_lshl_add_u32 v1, s2, 2, v1
	v_add_u32_e32 v1, s31, v1
	s_movk_i32 s2, 0xc35
	v_cmp_gt_i32_e32 vcc, s2, v1
	s_and_saveexec_b64 s[2:3], vcc
	s_cbranch_execz .LBB9_4
	s_load_dwordx4 s[4:7], s[0:1], 0x30
	s_load_dwordx2 s[2:3], s[0:1], 0x40
	s_load_dwordx4 s[8:11], s[0:1], 0x0
	v_and_b32_e32 v22, 31, v0
	v_lshlrev_b32_e32 v1, 5, v1
	v_or_b32_e32 v2, v1, v22
	v_ashrrev_i32_e32 v3, 31, v2
	v_lshlrev_b64 v[16:17], 7, v[2:3]
	v_and_b32_e32 v4, 32, v0
	s_waitcnt lgkmcnt(0)
	v_lshl_add_u64 v[2:3], s[10:11], 0, v[16:17]
	v_lshlrev_b32_e32 v28, 1, v4
	v_mov_b32_e32 v29, 0
	v_lshl_add_u64 v[18:19], v[2:3], 0, v[28:29]
	s_waitcnt vmcnt(0)
	v_mov_b32_e32 v2, v44
	v_mov_b32_e32 v3, v45
	v_mov_b32_e32 v4, v46
	v_mov_b32_e32 v5, v47
	v_mov_b32_e32 v6, v48
	v_mov_b32_e32 v7, v49
	v_mov_b32_e32 v8, v50
	v_mov_b32_e32 v9, v51
	v_mov_b32_e32 v12, v52
	v_mov_b32_e32 v13, v53
	v_mov_b32_e32 v14, v54
	v_mov_b32_e32 v15, v55
	v_mov_b32_e32 v24, v56
	v_mov_b32_e32 v25, v57
	v_mov_b32_e32 v26, v58
	v_mov_b32_e32 v27, v59
	v_lshl_add_u64 v[16:17], s[8:9], 0, v[16:17]
	v_lshl_add_u64 v[16:17], v[16:17], 0, v[28:29]
	v_and_b32_e32 v76, 0x80, v10
	v_and_b32_e32 v20, 63, v0
	v_lshrrev_b32_e32 v0, 3, v0
	v_and_or_b32 v0, v0, 4, v1
	v_ashrrev_i32_e32 v1, 31, v0
	s_waitcnt vmcnt(0)
	v_mov_b32_e32 v28, v60
	v_mov_b32_e32 v29, v61
	v_mov_b32_e32 v30, v62
	v_mov_b32_e32 v31, v63
	v_mov_b32_e32 v32, v64
	v_mov_b32_e32 v33, v65
	v_mov_b32_e32 v34, v66
	v_mov_b32_e32 v35, v67
	v_mov_b32_e32 v36, v68
	v_mov_b32_e32 v37, v69
	v_mov_b32_e32 v38, v70
	v_mov_b32_e32 v39, v71
	v_mov_b32_e32 v40, v72
	v_mov_b32_e32 v41, v73
	v_mov_b32_e32 v42, v74
	v_mov_b32_e32 v43, v75
	v_cvt_f32_f16_sdwa v17, v24 dst_sel:DWORD dst_unused:UNUSED_PAD src0_sel:WORD_1
	s_waitcnt vmcnt(0)
	v_lshlrev_b32_e32 v11, 16, v40
	v_and_b32_e32 v16, 0xffff0000, v40
	v_lshlrev_b32_e32 v21, 16, v41
	v_and_b32_e32 v23, 0xffff0000, v41
	v_lshlrev_b32_e32 v48, 16, v42
	v_and_b32_e32 v49, 0xffff0000, v42
	v_lshlrev_b32_e32 v50, 16, v43
	v_and_b32_e32 v51, 0xffff0000, v43
	v_lshlrev_b32_e32 v52, 16, v36
	v_and_b32_e32 v53, 0xffff0000, v36
	v_lshlrev_b32_e32 v54, 16, v37
	v_and_b32_e32 v55, 0xffff0000, v37
	v_lshlrev_b32_e32 v56, 16, v38
	v_and_b32_e32 v57, 0xffff0000, v38
	v_lshlrev_b32_e32 v58, 16, v39
	v_and_b32_e32 v59, 0xffff0000, v39
	v_lshlrev_b32_e32 v60, 16, v32
	v_and_b32_e32 v61, 0xffff0000, v32
	v_lshlrev_b32_e32 v62, 16, v33
	v_and_b32_e32 v63, 0xffff0000, v33
	v_lshlrev_b32_e32 v64, 16, v34
	v_and_b32_e32 v65, 0xffff0000, v34
	v_lshlrev_b32_e32 v66, 16, v35
	v_and_b32_e32 v67, 0xffff0000, v35
	v_lshlrev_b32_e32 v68, 16, v28
	v_and_b32_e32 v69, 0xffff0000, v28
	v_lshlrev_b32_e32 v70, 16, v29
	v_and_b32_e32 v71, 0xffff0000, v29
	v_lshlrev_b32_e32 v72, 16, v30
	v_and_b32_e32 v73, 0xffff0000, v30
	v_lshlrev_b32_e32 v74, 16, v31
	v_and_b32_e32 v75, 0xffff0000, v31
	ds_read_b128 v[28:31], v76 offset:32768
	ds_read_b128 v[32:35], v76 offset:32784
	ds_read_b128 v[36:39], v76 offset:32800
	ds_read_b128 v[40:43], v76 offset:32816
	ds_read_b128 v[44:47], v76 offset:33024
	s_waitcnt lgkmcnt(0)
	v_fma_f32 v10, v28, v11, v44
	v_fma_f32 v11, v29, v16, v45
	v_cvt_f32_f16_e32 v16, v24
	v_max_f32_e32 v10, 0, v10
	v_max_f32_e32 v11, 0, v11
	v_fmac_f32_e32 v47, v31, v23
	v_pk_add_f32 v[44:45], v[10:11], v[16:17]
	v_cvt_f32_f16_e32 v16, v25
	v_cvt_f32_f16_sdwa v17, v25 dst_sel:DWORD dst_unused:UNUSED_PAD src0_sel:WORD_1
	v_fma_f32 v10, v30, v21, v46
	ds_read_b128 v[28:31], v76 offset:33040
	v_max_f32_e32 v10, 0, v10
	v_max_f32_e32 v11, 0, v47
	v_pk_add_f32 v[46:47], v[10:11], v[16:17]
	v_cvt_f32_f16_e32 v16, v26
	v_cvt_f32_f16_sdwa v17, v26 dst_sel:DWORD dst_unused:UNUSED_PAD src0_sel:WORD_1
	s_waitcnt lgkmcnt(0)
	v_fma_f32 v10, v32, v48, v28
	v_fma_f32 v11, v33, v49, v29
	v_max_f32_e32 v10, 0, v10
	v_max_f32_e32 v11, 0, v11
	v_pk_add_f32 v[28:29], v[10:11], v[16:17]
	v_cvt_f32_f16_e32 v16, v27
	v_cvt_f32_f16_sdwa v17, v27 dst_sel:DWORD dst_unused:UNUSED_PAD src0_sel:WORD_1
	ds_read_b128 v[24:27], v76 offset:33056
	v_fma_f32 v10, v34, v50, v30
	v_fmac_f32_e32 v31, v35, v51
	v_max_f32_e32 v10, 0, v10
	v_max_f32_e32 v11, 0, v31
	v_pk_add_f32 v[30:31], v[10:11], v[16:17]
	v_cvt_f32_f16_e32 v16, v12
	v_cvt_f32_f16_sdwa v17, v12 dst_sel:DWORD dst_unused:UNUSED_PAD src0_sel:WORD_1
	s_waitcnt lgkmcnt(0)
	v_fma_f32 v10, v36, v52, v24
	v_fma_f32 v11, v37, v53, v25
	v_cvt_f32_f16_e32 v12, v13
	v_cvt_f32_f16_sdwa v13, v13 dst_sel:DWORD dst_unused:UNUSED_PAD src0_sel:WORD_1
	v_max_f32_e32 v10, 0, v10
	v_max_f32_e32 v11, 0, v11
	v_pk_add_f32 v[24:25], v[10:11], v[16:17]
	v_fma_f32 v10, v38, v54, v26
	v_fmac_f32_e32 v27, v39, v55
	v_max_f32_e32 v10, 0, v10
	v_max_f32_e32 v11, 0, v27
	v_pk_add_f32 v[26:27], v[10:11], v[12:13]
	ds_read_b128 v[10:13], v76 offset:33072
	v_cvt_f32_f16_e32 v16, v14
	v_cvt_f32_f16_sdwa v17, v14 dst_sel:DWORD dst_unused:UNUSED_PAD src0_sel:WORD_1
	v_lshlrev_b32_e32 v23, 4, v20
	s_waitcnt lgkmcnt(0)
	v_fma_f32 v10, v40, v56, v10
	v_fma_f32 v11, v41, v57, v11
	v_max_f32_e32 v10, 0, v10
	v_max_f32_e32 v11, 0, v11
	v_fmac_f32_e32 v13, v43, v59
	v_pk_add_f32 v[32:33], v[10:11], v[16:17]
	v_fma_f32 v10, v42, v58, v12
	v_max_f32_e32 v11, 0, v13
	v_cvt_f32_f16_e32 v12, v15
	v_cvt_f32_f16_sdwa v13, v15 dst_sel:DWORD dst_unused:UNUSED_PAD src0_sel:WORD_1
	v_max_f32_e32 v10, 0, v10
	v_pk_add_f32 v[34:35], v[10:11], v[12:13]
	ds_read_b128 v[10:13], v76 offset:32832
	ds_read_b128 v[14:17], v76 offset:33088
	s_waitcnt lgkmcnt(0)
	v_fma_f32 v10, v10, v60, v14
	v_fma_f32 v11, v11, v61, v15
	v_cvt_f32_f16_e32 v14, v6
	v_cvt_f32_f16_sdwa v15, v6 dst_sel:DWORD dst_unused:UNUSED_PAD src0_sel:WORD_1
	v_max_f32_e32 v10, 0, v10
	v_max_f32_e32 v11, 0, v11
	v_fma_f32 v6, v12, v62, v16
	v_pk_add_f32 v[36:37], v[10:11], v[14:15]
	v_max_f32_e32 v10, 0, v6
	v_cvt_f32_f16_e32 v6, v7
	v_cvt_f32_f16_sdwa v7, v7 dst_sel:DWORD dst_unused:UNUSED_PAD src0_sel:WORD_1
	v_fmac_f32_e32 v17, v13, v63
	v_max_f32_e32 v11, 0, v17
	v_pk_add_f32 v[38:39], v[10:11], v[6:7]
	ds_read_b128 v[10:13], v76 offset:32848
	ds_read_b128 v[14:17], v76 offset:33104
	s_waitcnt lgkmcnt(0)
	v_fma_f32 v6, v10, v64, v14
	v_fma_f32 v7, v11, v65, v15
	v_cvt_f32_f16_e32 v10, v8
	v_cvt_f32_f16_sdwa v11, v8 dst_sel:DWORD dst_unused:UNUSED_PAD src0_sel:WORD_1
	v_cvt_f32_f16_e32 v8, v9
	v_cvt_f32_f16_sdwa v9, v9 dst_sel:DWORD dst_unused:UNUSED_PAD src0_sel:WORD_1
	v_max_f32_e32 v6, 0, v6
	v_max_f32_e32 v7, 0, v7
	v_pk_add_f32 v[40:41], v[6:7], v[10:11]
	v_fma_f32 v6, v12, v66, v16
	v_fmac_f32_e32 v17, v13, v67
	v_max_f32_e32 v6, 0, v6
	v_max_f32_e32 v7, 0, v17
	v_pk_add_f32 v[42:43], v[6:7], v[8:9]
	ds_read_b128 v[6:9], v76 offset:32864
	ds_read_b128 v[10:13], v76 offset:33120
	v_cvt_pk_f16_f32 v14, v44, v45
	v_cvt_pk_f16_f32 v15, v46, v47
	v_cvt_pk_f16_f32 v16, v28, v29
	v_cvt_pk_f16_f32 v17, v30, v31
	s_waitcnt lgkmcnt(0)
	v_fma_f32 v6, v6, v68, v10
	v_fma_f32 v7, v7, v69, v11
	v_cvt_f32_f16_e32 v10, v2
	v_cvt_f32_f16_sdwa v11, v2 dst_sel:DWORD dst_unused:UNUSED_PAD src0_sel:WORD_1
	v_max_f32_e32 v6, 0, v6
	v_max_f32_e32 v7, 0, v7
	v_fma_f32 v2, v8, v70, v12
	v_pk_add_f32 v[48:49], v[6:7], v[10:11]
	v_max_f32_e32 v6, 0, v2
	v_cvt_f32_f16_e32 v2, v3
	v_cvt_f32_f16_sdwa v3, v3 dst_sel:DWORD dst_unused:UNUSED_PAD src0_sel:WORD_1
	v_fmac_f32_e32 v13, v9, v71
	v_max_f32_e32 v7, 0, v13
	v_pk_add_f32 v[50:51], v[6:7], v[2:3]
	ds_read_b128 v[6:9], v76 offset:32880
	ds_read_b128 v[10:13], v76 offset:33136
	global_store_dwordx4 v[18:19], v[14:17], off
	s_waitcnt lgkmcnt(0)
	v_fma_f32 v2, v6, v72, v10
	v_fma_f32 v3, v7, v73, v11
	v_cvt_f32_f16_e32 v6, v4
	v_cvt_f32_f16_sdwa v7, v4 dst_sel:DWORD dst_unused:UNUSED_PAD src0_sel:WORD_1
	v_cvt_f32_f16_e32 v4, v5
	v_cvt_f32_f16_sdwa v5, v5 dst_sel:DWORD dst_unused:UNUSED_PAD src0_sel:WORD_1
	v_max_f32_e32 v2, 0, v2
	v_max_f32_e32 v3, 0, v3
	v_pk_add_f32 v[52:53], v[2:3], v[6:7]
	v_fma_f32 v2, v8, v74, v12
	v_fmac_f32_e32 v13, v9, v75
	v_max_f32_e32 v2, 0, v2
	v_max_f32_e32 v3, 0, v13
	v_pk_add_f32 v[54:55], v[2:3], v[4:5]
	v_cvt_pk_f16_f32 v10, v24, v25
	v_cvt_pk_f16_f32 v11, v26, v27
	v_cvt_pk_f16_f32 v12, v32, v33
	v_cvt_pk_f16_f32 v13, v34, v35
	v_cvt_pk_f16_f32 v6, v36, v37
	v_cvt_pk_f16_f32 v7, v38, v39
	v_cvt_pk_f16_f32 v8, v40, v41
	v_cvt_pk_f16_f32 v9, v42, v43
	v_cvt_pk_f16_f32 v2, v48, v49
	v_cvt_pk_f16_f32 v3, v50, v51
	v_cvt_pk_f16_f32 v4, v52, v53
	v_cvt_pk_f16_f32 v5, v54, v55
	global_store_dwordx4 v[18:19], v[10:13], off offset:16
	global_store_dwordx4 v[18:19], v[6:9], off offset:32
	global_store_dwordx4 v[18:19], v[2:5], off offset:48
	v_lshlrev_b32_e32 v18, 3, v22
	global_load_dwordx2 a[0:1], v18, s[4:5]
	ds_read_b128 v[18:21], v23
	ds_read_b128 v[24:27], v23 offset:8192
	ds_read_b128 v[28:31], v23 offset:4096
	ds_read_b128 v[32:35], v23 offset:12288
	s_waitcnt vmcnt(0)
	v_accvgpr_mov_b32 a16, a0
	v_accvgpr_mov_b32 a17, a0
	v_accvgpr_mov_b32 a18, a0
	v_accvgpr_mov_b32 a19, a0
	v_accvgpr_mov_b32 a20, a0
	v_accvgpr_mov_b32 a21, a0
	v_accvgpr_mov_b32 a22, a0
	v_accvgpr_mov_b32 a23, a0
	v_accvgpr_mov_b32 a24, a0
	v_accvgpr_mov_b32 a25, a0
	v_accvgpr_mov_b32 a26, a0
	v_accvgpr_mov_b32 a27, a0
	v_accvgpr_mov_b32 a28, a0
	v_accvgpr_mov_b32 a29, a0
	v_accvgpr_mov_b32 a30, a0
	v_accvgpr_mov_b32 a31, a0
	v_accvgpr_mov_b32 a0, a1
	v_accvgpr_mov_b32 a2, a1
	v_accvgpr_mov_b32 a3, a1
	v_accvgpr_mov_b32 a4, a1
	v_accvgpr_mov_b32 a5, a1
	v_accvgpr_mov_b32 a6, a1
	v_accvgpr_mov_b32 a7, a1
	v_accvgpr_mov_b32 a8, a1
	v_accvgpr_mov_b32 a9, a1
	v_accvgpr_mov_b32 a10, a1
	v_accvgpr_mov_b32 a11, a1
	v_accvgpr_mov_b32 a12, a1
	v_accvgpr_mov_b32 a13, a1
	v_accvgpr_mov_b32 a14, a1
	v_accvgpr_mov_b32 a15, a1
	s_waitcnt lgkmcnt(3)
	v_mfma_f32_32x32x16_f16 a[16:31], v[14:17], v[18:21], a[16:31]
	s_waitcnt lgkmcnt(1)
	v_mfma_f32_32x32x16_f16 a[0:15], v[14:17], v[28:31], a[0:15]
	v_mfma_f32_32x32x16_f16 a[16:31], v[14:17], v[24:27], a[16:31]
	s_waitcnt lgkmcnt(0)
	v_mfma_f32_32x32x16_f16 a[0:15], v[14:17], v[32:35], a[0:15]
	ds_read_b128 v[18:21], v23 offset:1024
	ds_read_b128 v[24:27], v23 offset:9216
	ds_read_b128 v[28:31], v23 offset:5120
	ds_read_b128 v[32:35], v23 offset:13312
	s_waitcnt lgkmcnt(3)
	v_mfma_f32_32x32x16_f16 a[16:31], v[10:13], v[18:21], a[16:31]
	s_waitcnt lgkmcnt(1)
	v_mfma_f32_32x32x16_f16 a[0:15], v[10:13], v[28:31], a[0:15]
	v_mfma_f32_32x32x16_f16 a[16:31], v[10:13], v[24:27], a[16:31]
	s_waitcnt lgkmcnt(0)
	v_mfma_f32_32x32x16_f16 a[0:15], v[10:13], v[32:35], a[0:15]
	ds_read_b128 v[18:21], v23 offset:2048
	ds_read_b128 v[24:27], v23 offset:10240
	ds_read_b128 v[28:31], v23 offset:6144
	ds_read_b128 v[32:35], v23 offset:14336
	s_waitcnt lgkmcnt(3)
	v_mfma_f32_32x32x16_f16 a[16:31], v[6:9], v[18:21], a[16:31]
	s_waitcnt lgkmcnt(1)
	v_mfma_f32_32x32x16_f16 a[0:15], v[6:9], v[28:31], a[0:15]
	v_mfma_f32_32x32x16_f16 a[16:31], v[6:9], v[24:27], a[16:31]
	s_waitcnt lgkmcnt(0)
	v_mfma_f32_32x32x16_f16 a[0:15], v[6:9], v[32:35], a[0:15]
	ds_read_b128 v[18:21], v23 offset:3072
	ds_read_b128 v[24:27], v23 offset:11264
	ds_read_b128 v[28:31], v23 offset:7168
	ds_read_b128 v[32:35], v23 offset:15360
	s_waitcnt lgkmcnt(3)
	v_mfma_f32_32x32x16_f16 a[16:31], v[2:5], v[18:21], a[16:31]
	s_waitcnt lgkmcnt(1)
	v_mfma_f32_32x32x16_f16 a[0:15], v[2:5], v[28:31], a[0:15]
	v_mfma_f32_32x32x16_f16 a[16:31], v[2:5], v[24:27], a[16:31]
	s_waitcnt lgkmcnt(0)
	v_mfma_f32_32x32x16_f16 a[0:15], v[2:5], v[32:35], a[0:15]
	ds_read_b128 v[18:21], v23 offset:16384
	ds_read_b128 v[24:27], v23 offset:24576
	ds_read_b128 v[28:31], v23 offset:20480
	ds_read_b128 v[32:35], v23 offset:28672
	s_waitcnt lgkmcnt(3)
	v_mfma_f32_32x32x16_f16 a[32:47], v[14:17], v[18:21], 0
	s_waitcnt lgkmcnt(1)
	v_mfma_f32_32x32x16_f16 a[48:63], v[14:17], v[28:31], 0
	v_mfma_f32_32x32x16_f16 a[32:47], v[14:17], v[24:27], a[32:47]
	s_waitcnt lgkmcnt(0)
	v_mfma_f32_32x32x16_f16 a[48:63], v[14:17], v[32:35], a[48:63]
	ds_read_b128 v[14:17], v23 offset:17408
	ds_read_b128 v[18:21], v23 offset:25600
	ds_read_b128 v[24:27], v23 offset:21504
	ds_read_b128 v[28:31], v23 offset:29696
	s_waitcnt lgkmcnt(3)
	v_mfma_f32_32x32x16_f16 a[32:47], v[10:13], v[14:17], a[32:47]
	s_waitcnt lgkmcnt(1)
	v_mfma_f32_32x32x16_f16 a[48:63], v[10:13], v[24:27], a[48:63]
	v_mfma_f32_32x32x16_f16 a[32:47], v[10:13], v[18:21], a[32:47]
	s_waitcnt lgkmcnt(0)
	v_mfma_f32_32x32x16_f16 a[48:63], v[10:13], v[28:31], a[48:63]
	ds_read_b128 v[10:13], v23 offset:18432
	ds_read_b128 v[14:17], v23 offset:26624
	ds_read_b128 v[18:21], v23 offset:22528
	ds_read_b128 v[24:27], v23 offset:30720
	s_waitcnt lgkmcnt(3)
	v_mfma_f32_32x32x16_f16 a[32:47], v[6:9], v[10:13], a[32:47]
	s_waitcnt lgkmcnt(1)
	v_mfma_f32_32x32x16_f16 a[48:63], v[6:9], v[18:21], a[48:63]
	v_mfma_f32_32x32x16_f16 a[32:47], v[6:9], v[14:17], a[32:47]
	s_waitcnt lgkmcnt(0)
	v_mfma_f32_32x32x16_f16 a[48:63], v[6:9], v[24:27], a[48:63]
	ds_read_b128 v[10:13], v23 offset:19456
	ds_read_b128 v[6:9], v23 offset:27648
	ds_read_b128 v[18:21], v23 offset:23552
	ds_read_b128 v[14:17], v23 offset:31744
	s_waitcnt lgkmcnt(3)
	v_mfma_f32_32x32x16_f16 a[32:47], v[2:5], v[10:13], a[32:47]
	s_waitcnt lgkmcnt(1)
	v_mfma_f32_32x32x16_f16 a[48:63], v[2:5], v[18:21], a[48:63]
	v_mfma_f32_32x32x16_f16 a[32:47], v[2:5], v[6:9], a[32:47]
	v_lshlrev_b32_e32 v7, 2, v22
	s_waitcnt lgkmcnt(0)
	v_mfma_f32_32x32x16_f16 a[48:63], v[2:5], v[14:17], a[48:63]
	v_accvgpr_read_b32 v2, a0
	v_accvgpr_read_b32 v3, a16
	v_cvt_pk_bf16_f32 v6, v3, v2
	v_lshlrev_b64 v[2:3], 7, v[0:1]
	v_or_b32_e32 v2, v2, v7
	v_lshl_add_u64 v[4:5], s[6:7], 0, v[2:3]
	global_store_dword v[4:5], v6, off
	s_nop 1
	v_accvgpr_read_b32 v4, a32
	v_lshl_add_u64 v[2:3], s[2:3], 0, v[2:3]
	s_nop 0
	v_accvgpr_read_b32 v1, a48
	v_cvt_pk_bf16_f32 v1, v4, v1
	global_store_dword v[2:3], v1, off
	v_or_b32_e32 v2, 1, v0
	v_ashrrev_i32_e32 v3, 31, v2
	v_lshlrev_b64 v[2:3], 7, v[2:3]
	v_accvgpr_read_b32 v1, a1
	v_accvgpr_read_b32 v4, a17
	v_or_b32_e32 v2, v2, v7
	v_cvt_pk_bf16_f32 v1, v4, v1
	v_lshl_add_u64 v[4:5], s[6:7], 0, v[2:3]
	global_store_dword v[4:5], v1, off
	v_accvgpr_read_b32 v1, a49
	v_accvgpr_read_b32 v4, a33
	v_cvt_pk_bf16_f32 v1, v4, v1
	v_lshl_add_u64 v[2:3], s[2:3], 0, v[2:3]
	global_store_dword v[2:3], v1, off
	v_or_b32_e32 v2, 2, v0
	v_ashrrev_i32_e32 v3, 31, v2
	v_lshlrev_b64 v[2:3], 7, v[2:3]
	v_accvgpr_read_b32 v1, a2
	v_accvgpr_read_b32 v4, a18
	v_or_b32_e32 v2, v2, v7
	v_cvt_pk_bf16_f32 v1, v4, v1
	v_lshl_add_u64 v[4:5], s[6:7], 0, v[2:3]
	global_store_dword v[4:5], v1, off
	v_accvgpr_read_b32 v1, a50
	v_accvgpr_read_b32 v4, a34
	v_cvt_pk_bf16_f32 v1, v4, v1
	v_lshl_add_u64 v[2:3], s[2:3], 0, v[2:3]
	global_store_dword v[2:3], v1, off
	v_or_b32_e32 v2, 3, v0
	v_ashrrev_i32_e32 v3, 31, v2
	v_lshlrev_b64 v[2:3], 7, v[2:3]
	v_accvgpr_read_b32 v1, a3
	v_accvgpr_read_b32 v4, a19
	v_or_b32_e32 v2, v2, v7
	v_cvt_pk_bf16_f32 v1, v4, v1
	v_lshl_add_u64 v[4:5], s[6:7], 0, v[2:3]
	global_store_dword v[4:5], v1, off
	v_accvgpr_read_b32 v1, a51
	v_accvgpr_read_b32 v4, a35
	v_cvt_pk_bf16_f32 v1, v4, v1
	v_lshl_add_u64 v[2:3], s[2:3], 0, v[2:3]
	global_store_dword v[2:3], v1, off
	v_or_b32_e32 v2, 8, v0
	v_ashrrev_i32_e32 v3, 31, v2
	v_lshlrev_b64 v[2:3], 7, v[2:3]
	v_accvgpr_read_b32 v1, a4
	v_accvgpr_read_b32 v4, a20
	v_or_b32_e32 v2, v2, v7
	v_cvt_pk_bf16_f32 v1, v4, v1
	v_lshl_add_u64 v[4:5], s[6:7], 0, v[2:3]
	global_store_dword v[4:5], v1, off
	v_accvgpr_read_b32 v1, a52
	v_accvgpr_read_b32 v4, a36
	v_cvt_pk_bf16_f32 v1, v4, v1
	v_lshl_add_u64 v[2:3], s[2:3], 0, v[2:3]
	global_store_dword v[2:3], v1, off
	v_or_b32_e32 v2, 9, v0
	v_ashrrev_i32_e32 v3, 31, v2
	v_lshlrev_b64 v[2:3], 7, v[2:3]
	v_accvgpr_read_b32 v1, a5
	v_accvgpr_read_b32 v4, a21
	v_or_b32_e32 v2, v2, v7
	v_cvt_pk_bf16_f32 v1, v4, v1
	v_lshl_add_u64 v[4:5], s[6:7], 0, v[2:3]
	global_store_dword v[4:5], v1, off
	v_accvgpr_read_b32 v1, a53
	v_accvgpr_read_b32 v4, a37
	v_cvt_pk_bf16_f32 v1, v4, v1
	v_lshl_add_u64 v[2:3], s[2:3], 0, v[2:3]
	global_store_dword v[2:3], v1, off
	v_or_b32_e32 v2, 10, v0
	v_ashrrev_i32_e32 v3, 31, v2
	v_lshlrev_b64 v[2:3], 7, v[2:3]
	v_accvgpr_read_b32 v1, a6
	v_accvgpr_read_b32 v4, a22
	v_or_b32_e32 v2, v2, v7
	v_cvt_pk_bf16_f32 v1, v4, v1
	v_lshl_add_u64 v[4:5], s[6:7], 0, v[2:3]
	global_store_dword v[4:5], v1, off
	v_accvgpr_read_b32 v1, a54
	v_accvgpr_read_b32 v4, a38
	v_cvt_pk_bf16_f32 v1, v4, v1
	v_lshl_add_u64 v[2:3], s[2:3], 0, v[2:3]
	global_store_dword v[2:3], v1, off
	v_or_b32_e32 v2, 11, v0
	v_ashrrev_i32_e32 v3, 31, v2
	v_lshlrev_b64 v[2:3], 7, v[2:3]
	v_accvgpr_read_b32 v1, a7
	v_accvgpr_read_b32 v4, a23
	v_or_b32_e32 v2, v2, v7
	v_cvt_pk_bf16_f32 v1, v4, v1
	v_lshl_add_u64 v[4:5], s[6:7], 0, v[2:3]
	global_store_dword v[4:5], v1, off
	v_accvgpr_read_b32 v1, a55
	v_accvgpr_read_b32 v4, a39
	v_cvt_pk_bf16_f32 v1, v4, v1
	v_lshl_add_u64 v[2:3], s[2:3], 0, v[2:3]
	global_store_dword v[2:3], v1, off
	v_or_b32_e32 v2, 16, v0
	v_ashrrev_i32_e32 v3, 31, v2
	v_lshlrev_b64 v[2:3], 7, v[2:3]
	v_accvgpr_read_b32 v1, a8
	v_accvgpr_read_b32 v4, a24
	v_or_b32_e32 v2, v2, v7
	v_cvt_pk_bf16_f32 v1, v4, v1
	v_lshl_add_u64 v[4:5], s[6:7], 0, v[2:3]
	global_store_dword v[4:5], v1, off
	v_accvgpr_read_b32 v1, a56
	v_accvgpr_read_b32 v4, a40
	v_cvt_pk_bf16_f32 v1, v4, v1
	v_lshl_add_u64 v[2:3], s[2:3], 0, v[2:3]
	global_store_dword v[2:3], v1, off
	v_or_b32_e32 v2, 17, v0
	v_ashrrev_i32_e32 v3, 31, v2
	v_lshlrev_b64 v[2:3], 7, v[2:3]
	v_accvgpr_read_b32 v1, a9
	v_accvgpr_read_b32 v4, a25
	v_or_b32_e32 v2, v2, v7
	v_cvt_pk_bf16_f32 v1, v4, v1
	v_lshl_add_u64 v[4:5], s[6:7], 0, v[2:3]
	global_store_dword v[4:5], v1, off
	v_accvgpr_read_b32 v1, a57
	v_accvgpr_read_b32 v4, a41
	v_cvt_pk_bf16_f32 v1, v4, v1
	v_lshl_add_u64 v[2:3], s[2:3], 0, v[2:3]
	global_store_dword v[2:3], v1, off
	v_or_b32_e32 v2, 18, v0
	v_ashrrev_i32_e32 v3, 31, v2
	v_lshlrev_b64 v[2:3], 7, v[2:3]
	v_accvgpr_read_b32 v1, a10
	v_accvgpr_read_b32 v4, a26
	v_or_b32_e32 v2, v2, v7
	v_cvt_pk_bf16_f32 v1, v4, v1
	v_lshl_add_u64 v[4:5], s[6:7], 0, v[2:3]
	global_store_dword v[4:5], v1, off
	v_accvgpr_read_b32 v1, a58
	v_accvgpr_read_b32 v4, a42
	v_cvt_pk_bf16_f32 v1, v4, v1
	v_lshl_add_u64 v[2:3], s[2:3], 0, v[2:3]
	global_store_dword v[2:3], v1, off
	v_or_b32_e32 v2, 19, v0
	v_ashrrev_i32_e32 v3, 31, v2
	v_lshlrev_b64 v[2:3], 7, v[2:3]
	v_accvgpr_read_b32 v1, a11
	v_accvgpr_read_b32 v4, a27
	v_or_b32_e32 v2, v2, v7
	v_cvt_pk_bf16_f32 v1, v4, v1
	v_lshl_add_u64 v[4:5], s[6:7], 0, v[2:3]
	global_store_dword v[4:5], v1, off
	v_accvgpr_read_b32 v1, a59
	v_accvgpr_read_b32 v4, a43
	v_cvt_pk_bf16_f32 v1, v4, v1
	v_lshl_add_u64 v[2:3], s[2:3], 0, v[2:3]
	global_store_dword v[2:3], v1, off
	v_or_b32_e32 v2, 24, v0
	v_ashrrev_i32_e32 v3, 31, v2
	v_lshlrev_b64 v[2:3], 7, v[2:3]
	v_accvgpr_read_b32 v1, a12
	v_accvgpr_read_b32 v4, a28
	v_or_b32_e32 v2, v2, v7
	v_cvt_pk_bf16_f32 v1, v4, v1
	v_lshl_add_u64 v[4:5], s[6:7], 0, v[2:3]
	global_store_dword v[4:5], v1, off
	v_accvgpr_read_b32 v1, a60
	v_accvgpr_read_b32 v4, a44
	v_cvt_pk_bf16_f32 v1, v4, v1
	v_lshl_add_u64 v[2:3], s[2:3], 0, v[2:3]
	global_store_dword v[2:3], v1, off
	v_or_b32_e32 v2, 25, v0
	v_ashrrev_i32_e32 v3, 31, v2
	v_lshlrev_b64 v[2:3], 7, v[2:3]
	v_accvgpr_read_b32 v1, a13
	v_accvgpr_read_b32 v4, a29
	v_or_b32_e32 v2, v2, v7
	v_cvt_pk_bf16_f32 v1, v4, v1
	v_lshl_add_u64 v[4:5], s[6:7], 0, v[2:3]
	global_store_dword v[4:5], v1, off
	v_accvgpr_read_b32 v1, a61
	v_accvgpr_read_b32 v4, a45
	v_cvt_pk_bf16_f32 v1, v4, v1
	v_lshl_add_u64 v[2:3], s[2:3], 0, v[2:3]
	global_store_dword v[2:3], v1, off
	v_or_b32_e32 v2, 26, v0
	v_ashrrev_i32_e32 v3, 31, v2
	v_lshlrev_b64 v[2:3], 7, v[2:3]
	v_accvgpr_read_b32 v1, a14
	v_accvgpr_read_b32 v4, a30
	v_or_b32_e32 v2, v2, v7
	v_cvt_pk_bf16_f32 v1, v4, v1
	v_lshl_add_u64 v[4:5], s[6:7], 0, v[2:3]
	global_store_dword v[4:5], v1, off
	v_accvgpr_read_b32 v1, a62
	v_accvgpr_read_b32 v4, a46
	v_cvt_pk_bf16_f32 v1, v4, v1
	v_lshl_add_u64 v[2:3], s[2:3], 0, v[2:3]
	v_or_b32_e32 v0, 27, v0
	global_store_dword v[2:3], v1, off
	v_ashrrev_i32_e32 v1, 31, v0
	v_lshlrev_b64 v[0:1], 7, v[0:1]
	v_accvgpr_read_b32 v2, a15
	v_accvgpr_read_b32 v3, a31
	v_or_b32_e32 v0, v0, v7
	v_cvt_pk_bf16_f32 v4, v3, v2
	v_lshl_add_u64 v[2:3], s[6:7], 0, v[0:1]
	global_store_dword v[2:3], v4, off
	v_accvgpr_read_b32 v2, a63
	v_accvgpr_read_b32 v3, a47
	v_cvt_pk_bf16_f32 v2, v3, v2
	v_lshl_add_u64 v[0:1], s[2:3], 0, v[0:1]
	global_store_dword v[0:1], v2, off
	s_cmp_lg_u32 s31, 0
	s_cbranch_scc1 .LBB9_4
	s_mov_b64 exec, -1
	v_lshrrev_b32_e32 v78, 6, v77
	s_lshl_b32 s33, s30, 2
	v_readfirstlane_b32 s32, v78
	s_add_i32 s32, s32, s33
	s_cmp_ge_u32 s32, 53
	s_cbranch_scc1 .LBB9_4
	s_movk_i32 s31, 0xc00
	s_mov_b32 s2, s30
	v_mov_b32_e32 v0, v77
	v_mov_b32_e32 v10, v79
	s_add_i32 s32, s32, 0xc00
	s_lshl_b32 s32, s32, 5
	v_and_b32_e32 v78, 31, v0
	v_or_b32_e32 v78, s32, v78
	v_lshlrev_b32_e32 v78, 7, v78
	v_and_b32_e32 v1, 32, v0
	v_lshl_add_u32 v78, v1, 1, v78
	global_load_dwordx4 v[44:47], v78, s[22:23] offset:48
	global_load_dwordx4 v[48:51], v78, s[22:23] offset:32
	global_load_dwordx4 v[52:55], v78, s[22:23] offset:16
	global_load_dwordx4 v[56:59], v78, s[22:23]
	global_load_dwordx4 v[60:63], v78, s[20:21] offset:48
	global_load_dwordx4 v[64:67], v78, s[20:21] offset:32
	global_load_dwordx4 v[68:71], v78, s[20:21] offset:16
	global_load_dwordx4 v[72:75], v78, s[20:21]
	s_waitcnt vmcnt(0)
	s_branch .Lu3_again
